# v027 + every workgroup issues an L2 write-back (buffer_wbl2 sc1) on arrival at the grid barrier, so the XCD leader's release flush finds little dirty data
# baseline (speedup 1.0000x reference)
; #define LAS __attribute__((address_space(3)))
; __device__ __forceinline__ unsigned xb_add(unsigned* p, unsigned v) { return __hip_atomic_fetch_add(p, v, __ATOMIC_RELAXED, __HIP_MEMORY_SCOPE_AGENT); }
; __device__ __forceinline__ unsigned xb_xcc_id() { return (unsigned)__builtin_amdgcn_s_getreg((3 << 11) | 20) & 0xFu; }
; __global__ __launch_bounds__(NTHR, 2) void mega(Params p) {
;     extern __shared__ __attribute__((aligned(16))) unsigned char smem[];
;     LAS unsigned char* lds = (LAS unsigned char*)smem;
;     volatile LAS unsigned* st = (volatile LAS unsigned*)(lds + LDS_BYTES - 16);
;     if (threadIdx.x == 0) { st[0] = 0u; st[1] = 0u; st[2] = 0u; st[3] = 0u; }
;     __syncthreads();
;     XcdBarrier bar; bar.bar = WSP(unsigned, OFF_BAR); bar.x = xb_xcc_id(); bar.st = st;
;     if (threadIdx.x == 0) st[2] = xb_add(&bar.bar[XB_XCNT(bar.x)], 1u);
.LBB0_2:
	s_or_b64 exec, exec, s[4:5]
	s_waitcnt lgkmcnt(0)
	s_barrier
	s_getreg_b32 s3, hwreg(HW_REG_XCC_ID, 0, 4)
	s_and_b32 s95, s3, 15
	s_mov_b64 s[4:5], exec
	v_readlane_b32 s6, v250, 0
	v_readlane_b32 s7, v250, 1
	s_and_b64 s[6:7], s[4:5], s[6:7]
	s_mov_b64 exec, s[6:7]
	s_cbranch_execz .LBB0_6
	s_mov_b64 s[8:9], exec
	v_mbcnt_lo_u32_b32 v1, s8, 0
	v_mbcnt_hi_u32_b32 v1, s9, v1
	v_cmp_eq_u32_e32 vcc, 0, v1
	s_and_saveexec_b64 s[6:7], vcc
	s_cbranch_execz .LBB0_5
	s_lshl_b32 s3, s95, 8
	s_bcnt1_i32_b64 s8, s[8:9]
	v_mov_b32_e32 v2, s3
	v_mov_b32_e32 v3, s8
	buffer_wbl2 sc1
	s_waitcnt vmcnt(0)
	global_atomic_add v2, v2, v3, s[90:91] offset:1024 sc0

; __device__ __forceinline__ unsigned xb_add(unsigned* p, unsigned v) { return __hip_atomic_fetch_add(p, v, __ATOMIC_RELAXED, __HIP_MEMORY_SCOPE_AGENT); }
; __device__ __forceinline__ void xcd_barrier(const XcdBarrier& b) {
;     ...
;         unsigned* bar = b.bar;
;         __builtin_amdgcn_s_waitcnt(0);
;         unsigned nloc = b.st[0], nx = b.st[1];
;         if (nloc == 0u) { xcd_barrier_complete(bar, b.x, nloc, nx); b.st[0] = nloc; b.st[1] = nx; }
;         const unsigned old = xb_add(&bar[XB_XSUB(b.x)], 1u);
;         const unsigned gen = old / nloc;
.LBB0_78:
	s_mov_b64 s[8:9], exec
	s_lshl_b32 s3, s95, 8
	v_mbcnt_lo_u32_b32 v2, s8, 0
	s_add_u32 s6, s90, s3
	v_mbcnt_hi_u32_b32 v2, s9, v2
	s_addc_u32 s7, s91, 0
	v_cmp_eq_u32_e32 vcc, 0, v2
	s_and_saveexec_b64 s[10:11], vcc
	s_cbranch_execz .LBB0_80
	s_bcnt1_i32_b64 s3, s[8:9]
	v_mov_b32_e32 v4, 0x1000
	v_mov_b32_e32 v5, s3
	buffer_wbl2 sc1
	s_waitcnt vmcnt(0)
	global_atomic_add v4, v4, v5, s[6:7] offset:1024 sc0

; __device__ __forceinline__ unsigned xb_add(unsigned* p, unsigned v) { return __hip_atomic_fetch_add(p, v, __ATOMIC_RELAXED, __HIP_MEMORY_SCOPE_AGENT); }
; __device__ __forceinline__ void xcd_barrier(const XcdBarrier& b) {
;     ...
;         if (old + 1u == (gen + 1u) * nloc) {
;             __builtin_amdgcn_fence(__ATOMIC_RELEASE, "agent");
;             asm volatile("s_waitcnt vmcnt(0)" ::: "memory");
;             const unsigned og = xb_add(&bar[XB_TOP], 1u);
.LBB0_94:
	s_andn2_saveexec_b64 s[8:9], s[8:9]
	s_cbranch_execz .LBB0_114
	s_mov_b64 s[8:9], exec
	buffer_wbl2 sc1
	s_waitcnt lgkmcnt(0)
	s_waitcnt vmcnt(0)
	v_mbcnt_lo_u32_b32 v2, s8, 0
	v_mbcnt_hi_u32_b32 v2, s9, v2
	v_cmp_eq_u32_e32 vcc, 0, v2
	s_and_saveexec_b64 s[10:11], vcc
	s_cbranch_execz .LBB0_97
	s_bcnt1_i32_b64 s3, s[8:9]
	v_mov_b32_e32 v3, 0x3000
	v_mov_b32_e32 v4, s3
	buffer_wbl2 sc1
	s_waitcnt vmcnt(0)
	global_atomic_add v3, v3, v4, s[90:91] offset:1024 sc0

; __device__ __forceinline__ unsigned xb_add(unsigned* p, unsigned v) { return __hip_atomic_fetch_add(p, v, __ATOMIC_RELAXED, __HIP_MEMORY_SCOPE_AGENT); }
; __device__ __forceinline__ void xcd_barrier(const XcdBarrier& b) {
;     ...
;         unsigned* bar = b.bar;
;         __builtin_amdgcn_s_waitcnt(0);
;         unsigned nloc = b.st[0], nx = b.st[1];
;         if (nloc == 0u) { xcd_barrier_complete(bar, b.x, nloc, nx); b.st[0] = nloc; b.st[1] = nx; }
;         const unsigned old = xb_add(&bar[XB_XSUB(b.x)], 1u);
;         const unsigned gen = old / nloc;
.LBB0_139:
	s_mov_b64 s[4:5], exec
	s_lshl_b32 s2, s95, 8
	v_mbcnt_lo_u32_b32 v2, s4, 0
	s_add_u32 s2, s90, s2
	v_mbcnt_hi_u32_b32 v2, s5, v2
	s_addc_u32 s3, s91, 0
	v_cmp_eq_u32_e32 vcc, 0, v2
	s_and_saveexec_b64 s[6:7], vcc
	s_cbranch_execz .LBB0_141
	s_bcnt1_i32_b64 s4, s[4:5]
	v_mov_b32_e32 v4, 0x1000
	v_mov_b32_e32 v5, s4
	buffer_wbl2 sc1
	s_waitcnt vmcnt(0)
	global_atomic_add v4, v4, v5, s[2:3] offset:1024 sc0

; __device__ __forceinline__ unsigned xb_add(unsigned* p, unsigned v) { return __hip_atomic_fetch_add(p, v, __ATOMIC_RELAXED, __HIP_MEMORY_SCOPE_AGENT); }
; __device__ __forceinline__ void xcd_barrier(const XcdBarrier& b) {
;     ...
;         if (old + 1u == (gen + 1u) * nloc) {
;             __builtin_amdgcn_fence(__ATOMIC_RELEASE, "agent");
;             asm volatile("s_waitcnt vmcnt(0)" ::: "memory");
;             const unsigned og = xb_add(&bar[XB_TOP], 1u);
.LBB0_155:
	s_andn2_saveexec_b64 s[4:5], s[4:5]
	s_cbranch_execz .LBB0_175
	s_mov_b64 s[4:5], exec
	buffer_wbl2 sc1
	s_waitcnt lgkmcnt(0)
	s_waitcnt vmcnt(0)
	v_mbcnt_lo_u32_b32 v2, s4, 0
	v_mbcnt_hi_u32_b32 v2, s5, v2
	v_cmp_eq_u32_e32 vcc, 0, v2
	s_and_saveexec_b64 s[6:7], vcc
	s_cbranch_execz .LBB0_158
	s_bcnt1_i32_b64 s4, s[4:5]
	v_mov_b32_e32 v3, 0x3000
	v_mov_b32_e32 v4, s4
	buffer_wbl2 sc1
	s_waitcnt vmcnt(0)
	global_atomic_add v3, v3, v4, s[90:91] offset:1024 sc0

; __device__ __forceinline__ unsigned xb_add(unsigned* p, unsigned v) { return __hip_atomic_fetch_add(p, v, __ATOMIC_RELAXED, __HIP_MEMORY_SCOPE_AGENT); }
; __device__ __forceinline__ void xcd_barrier(const XcdBarrier& b) {
;     ...
;         unsigned* bar = b.bar;
;         __builtin_amdgcn_s_waitcnt(0);
;         unsigned nloc = b.st[0], nx = b.st[1];
;         if (nloc == 0u) { xcd_barrier_complete(bar, b.x, nloc, nx); b.st[0] = nloc; b.st[1] = nx; }
;         const unsigned old = xb_add(&bar[XB_XSUB(b.x)], 1u);
;         const unsigned gen = old / nloc;
.LBB0_239:
	s_mov_b64 s[12:13], exec
	s_lshl_b32 s4, s95, 8
	v_mbcnt_lo_u32_b32 v2, s12, 0
	s_add_u32 s4, s90, s4
	v_mbcnt_hi_u32_b32 v2, s13, v2
	s_addc_u32 s5, s91, 0
	v_cmp_eq_u32_e32 vcc, 0, v2
	s_and_saveexec_b64 s[14:15], vcc
	s_cbranch_execz .LBB0_241
	s_bcnt1_i32_b64 s12, s[12:13]
	v_mov_b32_e32 v4, 0x1000
	v_mov_b32_e32 v5, s12
	buffer_wbl2 sc1
	s_waitcnt vmcnt(0)
	global_atomic_add v4, v4, v5, s[4:5] offset:1024 sc0

; __device__ __forceinline__ unsigned xb_add(unsigned* p, unsigned v) { return __hip_atomic_fetch_add(p, v, __ATOMIC_RELAXED, __HIP_MEMORY_SCOPE_AGENT); }
; __device__ __forceinline__ void xcd_barrier(const XcdBarrier& b) {
;     ...
;         if (old + 1u == (gen + 1u) * nloc) {
;             __builtin_amdgcn_fence(__ATOMIC_RELEASE, "agent");
;             asm volatile("s_waitcnt vmcnt(0)" ::: "memory");
;             const unsigned og = xb_add(&bar[XB_TOP], 1u);
.LBB0_255:
	s_andn2_saveexec_b64 s[12:13], s[12:13]
	s_cbranch_execz .LBB0_275
	s_mov_b64 s[12:13], exec
	buffer_wbl2 sc1
	s_waitcnt lgkmcnt(0)
	s_waitcnt vmcnt(0)
	v_mbcnt_lo_u32_b32 v2, s12, 0
	v_mbcnt_hi_u32_b32 v2, s13, v2
	v_cmp_eq_u32_e32 vcc, 0, v2
	s_and_saveexec_b64 s[14:15], vcc
	s_cbranch_execz .LBB0_258
	s_bcnt1_i32_b64 s12, s[12:13]
	v_mov_b32_e32 v3, 0x3000
	v_mov_b32_e32 v4, s12
	buffer_wbl2 sc1
	s_waitcnt vmcnt(0)
	global_atomic_add v3, v3, v4, s[90:91] offset:1024 sc0

; __device__ __forceinline__ unsigned xb_add(unsigned* p, unsigned v) { return __hip_atomic_fetch_add(p, v, __ATOMIC_RELAXED, __HIP_MEMORY_SCOPE_AGENT); }
; __device__ __forceinline__ void xcd_barrier(const XcdBarrier& b) {
;     ...
;         unsigned* bar = b.bar;
;         __builtin_amdgcn_s_waitcnt(0);
;         unsigned nloc = b.st[0], nx = b.st[1];
;         if (nloc == 0u) { xcd_barrier_complete(bar, b.x, nloc, nx); b.st[0] = nloc; b.st[1] = nx; }
;         const unsigned old = xb_add(&bar[XB_XSUB(b.x)], 1u);
;         const unsigned gen = old / nloc;
.LBB0_1210:
	s_mov_b64 s[6:7], exec
	s_lshl_b32 s2, s95, 8
	v_mbcnt_lo_u32_b32 v2, s6, 0
	s_add_u32 s2, s90, s2
	v_mbcnt_hi_u32_b32 v2, s7, v2
	s_addc_u32 s3, s91, 0
	v_cmp_eq_u32_e32 vcc, 0, v2
	s_and_saveexec_b64 s[8:9], vcc
	s_cbranch_execz .LBB0_1212
	s_bcnt1_i32_b64 s6, s[6:7]
	v_mov_b32_e32 v4, 0x1000
	v_mov_b32_e32 v5, s6
	buffer_wbl2 sc1
	s_waitcnt vmcnt(0)
	global_atomic_add v4, v4, v5, s[2:3] offset:1024 sc0

; __device__ __forceinline__ unsigned xb_add(unsigned* p, unsigned v) { return __hip_atomic_fetch_add(p, v, __ATOMIC_RELAXED, __HIP_MEMORY_SCOPE_AGENT); }
; __device__ __forceinline__ void xcd_barrier(const XcdBarrier& b) {
;     ...
;         if (old + 1u == (gen + 1u) * nloc) {
;             __builtin_amdgcn_fence(__ATOMIC_RELEASE, "agent");
;             asm volatile("s_waitcnt vmcnt(0)" ::: "memory");
;             const unsigned og = xb_add(&bar[XB_TOP], 1u);
.LBB0_1226:
	s_andn2_saveexec_b64 s[6:7], s[6:7]
	s_cbranch_execz .LBB0_1246
	s_mov_b64 s[6:7], exec
	buffer_wbl2 sc1
	s_waitcnt lgkmcnt(0)
	s_waitcnt vmcnt(0)
	v_mbcnt_lo_u32_b32 v2, s6, 0
	v_mbcnt_hi_u32_b32 v2, s7, v2
	v_cmp_eq_u32_e32 vcc, 0, v2
	s_and_saveexec_b64 s[8:9], vcc
	s_cbranch_execz .LBB0_1229
	s_bcnt1_i32_b64 s6, s[6:7]
	v_mov_b32_e32 v3, 0x3000
	v_mov_b32_e32 v4, s6
	buffer_wbl2 sc1
	s_waitcnt vmcnt(0)
	global_atomic_add v3, v3, v4, s[90:91] offset:1024 sc0
